# adds: P9 unit-top lookups off the critical path (scalar loads a unit ahead, token gather consumed inside the K-loop); P3 order pooling-first; pool stride = grid size
# speedup vs baseline: 1.0456x; 1.0047x over previous
; #define LAS __attribute__((address_space(3)))
; #define RUNPH(k, ...) do { if (IN(k)) { { PH_IDS __VA_ARGS__ } if (REP_PHASE == (k)) { xcd_barrier(bar); { PH_IDS __VA_ARGS__ } } SEAM(k); } } while (0)
; __device__ __forceinline__ void prep_item(const Args& a, LAS unsigned char* lds, int tid, int dir, int b, int ch) {
;     unsigned char* ws = a.ws;
;     const bf16* Q = (const bf16*)(ws + RA_Q); const bf16* Kb = (const bf16*)(ws + RA_K); const float* ALR = (const float*)(ws + RA_ALR);
;     v4u* QG = (v4u*)(ws + PQG); bf16* AM = (bf16*)(ws + PAM); bf16* KD = (bf16*)(ws + PKD); float* DEC = (float*)(ws + PDEC);
;     constexpr int TS = 520;
;     LAS float* alr = (LAS float*)lds;
;     LAS bf16* Kt = (LAS bf16*)(lds + 4096);
;     LAS bf16* Qt = (LAS bf16*)(lds + 4096 + 64 * TS * 2);
;     const int col = tid, h = col >> 7, dk = col & 127;
;     const int lane = tid & 63, wave = __builtin_amdgcn_readfirstlane(tid >> 6), l15 = lane & 15, l4 = lane >> 4;
;     const bool lat = ch >= 4;
;     if (tid < 256) { const int i = tid >> 2, r4 = (tid & 3) * 4; const int row = scan_row(b, dir, ch * 64 + i);
;         *(LAS f32x4*)(alr + i * 16 + r4) = *(const f32x4*)(ALR + (size_t)row * 32 + dir * 16 + r4); }
;     { v4u kr[8], qr[8];
; #pragma unroll
;       for (int q = 0; q < 8; ++q) { const int p = tid + 512 * q, i = p >> 6, c8 = (p & 63) * 8; const int row = scan_row(b, dir, ch * 64 + i);
;           kr[q] = *(const v4u*)(Kb + (size_t)row * 512 + c8); if (lat) qr[q] = *(const v4u*)(Q + (size_t)row * 512 + c8); }
; #pragma unroll
;       for (int q = 0; q < 8; ++q) { const int p = tid + 512 * q, i = p >> 6, c8 = (p & 63) * 8; *(LAS v4u*)(Kt + i * TS + c8) = kr[q]; if (lat) *(LAS v4u*)(Qt + i * TS + c8) = qr[q]; } }
;     const float* wa2 = dir ? a.in[13] : a.in[11]; const float bia = (dir ? a.in[14] : a.in[12])[col];
; __global__ void __launch_bounds__(512, 2) fwd(Args args) {
;     ...
;     RUNPH(3, for (int r_ = 0; r_ < P3_REP_PREP; ++r_) phase3_prep(args, lds, tid, vcu, G, bx); for (int r_ = 0; r_ < P3_REP_POOL; ++r_) phase3_pool(args, lds, tid, vcu, G););
.LBB0_316:
	s_cmp_gt_i32 s94, 3
	s_cselect_b64 s[0:1], -1, 0
	s_cmp_lt_i32 s95, 4
	s_cselect_b64 s[2:3], -1, 0
	s_or_b64 s[0:1], s[0:1], s[2:3]
	s_and_b64 vcc, exec, s[0:1]
	s_cbranch_vccnz .LBB0_764
	v_mov_b32_e32 v66, v0
	s_mov_b32 s99, 0
	s_branch .LBB0_673
.Lp3_prep_start:
	s_movk_i32 s2, 0xff
	v_lshlrev_b32_e32 v80, 2, v66
	v_ashrrev_i32_e32 v82, 2, v66
	v_and_b32_e32 v3, 12, v80
	v_lshlrev_b32_e32 v4, 6, v82
	v_lshlrev_b32_e32 v68, 2, v3
	v_lshlrev_b32_e32 v13, 4, v66
	s_add_i32 s24, 0, 0x11400
	v_cmp_lt_i32_e64 s[6:7], s2, v66
	v_add3_u32 v83, 0, v4, v68
	v_ashrrev_i32_e32 v84, 6, v66
	v_add_u32_e32 v4, 0x200, v66
	v_and_b32_e32 v6, 0x3f0, v13
	s_movk_i32 s2, 0x410
	v_ashrrev_i32_e32 v85, 6, v4
	v_add_u32_e32 v7, 0x400, v66
	v_add_u32_e32 v40, 0, v6
	v_add_u32_e32 v3, s24, v6
	v_mul_lo_u32 v14, v84, s2
	v_ashrrev_i32_e32 v86, 6, v7
	v_add_u32_e32 v8, 0x600, v66
	v_add_u32_e32 v92, v40, v14
	v_add_u32_e32 v93, v3, v14
	v_mul_lo_u32 v14, v85, s2
	v_ashrrev_i32_e32 v87, 6, v8
	v_add_u32_e32 v9, 0x800, v66
	v_add_u32_e32 v94, v40, v14
	v_add_u32_e32 v95, v3, v14
	v_mul_lo_u32 v14, v86, s2
	v_ashrrev_i32_e32 v88, 6, v9
	v_add_u32_e32 v10, 0xa00, v66
	v_add_u32_e32 v96, v40, v14
	v_add_u32_e32 v97, v3, v14
	v_mul_lo_u32 v14, v87, s2
	v_ashrrev_i32_e32 v89, 6, v10
	v_add_u32_e32 v11, 0xc00, v66
	v_add_u32_e32 v98, v40, v14
	v_add_u32_e32 v99, v3, v14
	v_mul_lo_u32 v14, v88, s2
	v_ashrrev_i32_e32 v90, 6, v11
	v_add_u32_e32 v12, 0xe00, v66
	v_add_u32_e32 v100, v40, v14
	v_add_u32_e32 v101, v3, v14
	v_mul_lo_u32 v14, v89, s2
	v_ashrrev_i32_e32 v91, 6, v12
	v_add_u32_e32 v102, v40, v14
	v_add_u32_e32 v103, v3, v14
	v_mul_lo_u32 v14, v90, s2
	v_add_u32_e32 v104, v40, v14
	v_add_u32_e32 v105, v3, v14
	v_mul_lo_u32 v14, v91, s2
	v_add_u32_e32 v106, v40, v14
	v_add_u32_e32 v107, v3, v14
	v_lshlrev_b32_e32 v14, 1, v66
	v_ashrrev_i32_e32 v16, 3, v66
	v_add_u32_e32 v108, 0, v14
	v_add_u32_e32 v110, s24, v14
	v_bfe_u32 v14, v66, 4, 6
	v_mov_b32_e32 v15, s24
	v_lshlrev_b32_e32 v16, 1, v16
	v_mad_u32_u24 v14, v14, s2, v15
	v_and_b32_e32 v16, 0xffffff00, v16
	v_and_b32_e32 v13, 0xf0, v13
	v_add3_u32 v187, v14, v16, v13
	v_bfe_u32 v16, v4, 4, 6
	v_ashrrev_i32_e32 v4, 3, v4
	v_lshlrev_b32_e32 v4, 1, v4
	v_mad_u32_u24 v16, v16, s2, v15
	v_and_b32_e32 v4, 0xffffff00, v4
	v_add3_u32 v188, v16, v4, v13
	v_ashrrev_i32_e32 v4, 3, v7
	v_lshlrev_b32_e32 v4, 1, v4
	v_and_b32_e32 v4, 0xffffff00, v4
	v_ashrrev_i32_e32 v7, 3, v8
	v_add3_u32 v189, v14, v4, v13
	v_bfe_u32 v4, v8, 4, 6
	v_lshlrev_b32_e32 v7, 1, v7
	v_mad_u32_u24 v4, v4, s2, v15
	v_and_b32_e32 v7, 0xffffff00, v7
	v_add3_u32 v190, v4, v7, v13
	v_ashrrev_i32_e32 v4, 3, v9
	v_lshlrev_b32_e32 v4, 1, v4
	v_and_b32_e32 v4, 0xffffff00, v4
	v_ashrrev_i32_e32 v7, 3, v10
	v_add3_u32 v191, v14, v4, v13
	v_bfe_u32 v4, v10, 4, 6
	v_lshlrev_b32_e32 v7, 1, v7
	v_mad_u32_u24 v4, v4, s2, v15
	v_and_b32_e32 v7, 0xffffff00, v7
	v_add3_u32 v192, v4, v7, v13
	v_ashrrev_i32_e32 v4, 3, v11
	v_lshlrev_b32_e32 v4, 1, v4
	v_and_b32_e32 v4, 0xffffff00, v4
	v_ashrrev_i32_e32 v7, 3, v12
	v_add3_u32 v193, v14, v4, v13
	v_bfe_u32 v4, v12, 4, 6
	v_lshlrev_b32_e32 v7, 1, v7
	s_add_u32 s12, s92, 0x30b00000
	v_mov_b32_e32 v5, 0
	v_mad_u32_u24 v4, v4, s2, v15
	v_and_b32_e32 v7, 0xffffff00, v7
	s_addc_u32 s13, s93, 0
	v_ashrrev_i32_e32 v2, 7, v66
	v_add3_u32 v194, v4, v7, v13
	v_mov_b32_e32 v7, v5
	s_add_u32 s25, s92, 0x32b00000
	v_ashrrev_i32_e32 v3, 31, v2
	v_lshl_add_u64 v[6:7], s[92:93], 0, v[6:7]
	s_mov_b64 s[2:3], 0x23200000
	s_addc_u32 s26, s93, 0
	v_ashrrev_i32_e32 v67, 31, v66
	v_lshlrev_b64 v[2:3], 14, v[2:3]
	v_lshlrev_b32_e32 v4, 7, v66
	v_lshl_add_u64 v[70:71], v[6:7], 0, s[2:3]
	s_mov_b64 s[2:3], 0x22200000
	s_add_u32 s10, s92, 0x2a800000
	v_bfe_u32 v1, v66, 4, 2
	v_and_b32_e32 v4, 0x3f80, v4
	v_lshl_add_u64 v[72:73], v[6:7], 0, s[2:3]
	v_lshl_add_u64 v[6:7], v[66:67], 2, s[92:93]
	s_mov_b64 s[2:3], 0x38f00000
	v_lshl_add_u64 v[2:3], s[92:93], 0, v[2:3]
	s_addc_u32 s11, s93, 0
	s_movk_i32 s0, 0x100
	v_and_b32_e32 v81, 15, v66
	v_lshlrev_b32_e32 v175, 2, v1
	v_lshl_add_u64 v[74:75], v[6:7], 0, s[2:3]
	v_lshl_add_u64 v[2:3], v[2:3], 0, v[4:5]
	s_mov_b64 s[2:3], 0x36b00000
	s_cmpk_lg_i32 s97, 0x100
	v_cmp_gt_i32_e64 s[0:1], s0, v66
	v_add_u32_e32 v109, 0x1000, v108
	v_add_u32_e32 v111, 0x410, v110
	v_add_u32_e32 v112, 0x820, v110
	v_add_u32_e32 v113, 0xc30, v110
	v_add_u32_e32 v114, 0x1040, v110
	v_add_u32_e32 v115, 0x1450, v110
	v_add_u32_e32 v116, 0x1860, v110
	v_add_u32_e32 v117, 0x1c70, v110
	v_add_u32_e32 v118, 0x2080, v110
	v_add_u32_e32 v119, 0x2490, v110
	v_add_u32_e32 v120, 0x28a0, v110
	v_add_u32_e32 v121, 0x2cb0, v110
	v_add_u32_e32 v122, 0x30c0, v110
	v_add_u32_e32 v123, 0x34d0, v110
	v_add_u32_e32 v124, 0x38e0, v110
	v_add_u32_e32 v125, 0x3cf0, v110
	v_add_u32_e32 v126, 0x4100, v110
	v_add_u32_e32 v127, 0x4510, v110
	v_add_u32_e32 v128, 0x4920, v110
	v_add_u32_e32 v129, 0x4d30, v110
	v_add_u32_e32 v130, 0x5140, v110
	v_add_u32_e32 v131, 0x5550, v110
	v_add_u32_e32 v132, 0x5960, v110
	v_add_u32_e32 v133, 0x5d70, v110
	v_add_u32_e32 v134, 0x6180, v110
	v_add_u32_e32 v135, 0x6590, v110
	v_add_u32_e32 v136, 0x69a0, v110
	v_add_u32_e32 v137, 0x6db0, v110
	v_add_u32_e32 v138, 0x71c0, v110
	v_add_u32_e32 v139, 0x75d0, v110
	v_add_u32_e32 v140, 0x79e0, v110
	v_add_u32_e32 v141, 0x7df0, v110
	v_add_u32_e32 v142, 0x8200, v110
	v_add_u32_e32 v143, 0x8610, v110
	v_add_u32_e32 v144, 0x8a20, v110
	v_add_u32_e32 v145, 0x8e30, v110
	v_add_u32_e32 v146, 0x9240, v110
	v_add_u32_e32 v147, 0x9650, v110
	v_add_u32_e32 v148, 0x9a60, v110
	v_add_u32_e32 v149, 0x9e70, v110
	v_add_u32_e32 v150, 0xa280, v110
	v_add_u32_e32 v151, 0xa690, v110
	v_add_u32_e32 v152, 0xaaa0, v110
	v_add_u32_e32 v153, 0xaeb0, v110
	v_add_u32_e32 v154, 0xb2c0, v110
	v_add_u32_e32 v155, 0xb6d0, v110
	v_add_u32_e32 v156, 0xbae0, v110
	v_add_u32_e32 v157, 0xbef0, v110
	v_add_u32_e32 v158, 0xc300, v110
	v_add_u32_e32 v159, 0xc710, v110
	v_add_u32_e32 v160, 0xcb20, v110
	v_add_u32_e32 v161, 0xcf30, v110
	v_add_u32_e32 v162, 0xd340, v110
	v_add_u32_e32 v163, 0xd750, v110
	v_add_u32_e32 v164, 0xdb60, v110
	v_add_u32_e32 v165, 0xdf70, v110
	v_add_u32_e32 v166, 0xe380, v110
	v_add_u32_e32 v167, 0xe790, v110
	v_add_u32_e32 v168, 0xeba0, v110
	v_add_u32_e32 v169, 0xefb0, v110
	v_add_u32_e32 v170, 0xf3c0, v110
	v_add_u32_e32 v171, 0xf7d0, v110
	v_add_u32_e32 v172, 0xfbe0, v110
	v_add_u32_e32 v173, 0xfff0, v110
	v_lshlrev_b32_e32 v174, 3, v1
	v_mul_u32_u24_e32 v1, 0x410, v81
	v_or_b32_e32 v176, 2, v175
	v_or_b32_e32 v177, 3, v175
	v_or_b32_e32 v178, 16, v175
	v_or_b32_e32 v179, 18, v175
	v_or_b32_e32 v180, 19, v175
	v_or_b32_e32 v181, 32, v175
	v_or_b32_e32 v182, 34, v175
	v_or_b32_e32 v183, 35, v175
	v_or_b32_e32 v184, 48, v175
	v_or_b32_e32 v185, 50, v175
	v_or_b32_e32 v186, 51, v175
	v_lshl_add_u64 v[76:77], v[2:3], 0, s[2:3]
	s_mov_b64 s[2:3], -1
	s_cbranch_scc0 .LBB0_337
; #define LAS __attribute__((address_space(3)))
; __device__ __forceinline__ void prep_item(const Args& a, LAS unsigned char* lds, int tid, int dir, int b, int ch) {
;     ...
;     float Gv[64]; float Gc = 0.f;
; #pragma unroll
;     for (int i = 0; i < 64; ++i) { float zp[4];
; #pragma unroll
;         for (int r4 = 0; r4 < 4; ++r4) { const f32x4 x = *(const LAS f32x4*)(alr + i * 16 + 4 * r4); zp[r4] = x[0] * w[4 * r4] + x[1] * w[4 * r4 + 1] + x[2] * w[4 * r4 + 2] + x[3] * w[4 * r4 + 3]; }
;         const float z = bia + ((zp[0] + zp[1]) + (zp[2] + zp[3]));
;         Gc += fminf(z, 0.f) * (L2E / 16.f) - __builtin_amdgcn_logf(1.f + __builtin_amdgcn_exp2f(-fabsf(z) * L2E)) * (1.f / 16.f); Gv[i] = Gc; }
;     const float Gmid = Gv[32], Gend = Gv[63];
;     DEC[((size_t)(dir * 8 + b) * 36 + ch) * 512 + col] = __builtin_amdgcn_exp2f(Gend);
; __device__ __forceinline__ void phase3_prep(const Args& a, LAS unsigned char* lds, int tid, int vcu, int G, int bx) {
;     ...
;     for (int item = vcu; item < 2 * 8 * 32; item += G) { const int lc = item & 31, b = (item >> 5) & 7, dir = item >> 8; prep_item(a, lds, tid, dir, b, 4 + lc); }
	v_readlane_b32 s2, v246, 2
	s_cmpk_gt_i32 s2, 0x1ff
	s_cbranch_scc1 .LBB0_329
	v_mov_b32_e32 v69, 0
	s_mov_b32 s14, 0x3db8aa3b
	v_add_u32_e32 v41, 0, v1
	v_lshl_add_u64 v[2:3], v[66:67], 4, s[12:13]
	v_lshl_add_u32 v42, v66, 1, 0
	s_movk_i32 s20, 0xff
	s_movk_i32 s21, 0x100
	s_movk_i32 s22, 0x4000
	v_mov_b32_e32 v43, 0x8ff
	v_mov_b32_e32 v44, 0xff
	v_lshlrev_b64 v[4:5], 2, v[66:67]
	s_movk_i32 s23, 0x1000
	s_movk_i32 s27, 0x2000
	s_movk_i32 s28, 0x3000
	s_movk_i32 s29, 0x5000
	s_movk_i32 s30, 0x6000
	s_movk_i32 s31, 0x7000
	s_mov_b32 s34, 0xbfb8aa3b
	s_mov_b32 s15, 0x3d800000
	s_movk_i32 s35, 0x7fff
	s_mov_b32 s58, 0xffff0000
	v_lshlrev_b32_e32 v6, 1, v175
	v_mov_b32_e32 v7, v69
	v_mov_b32_e32 v226, v69
	v_mov_b32_e32 v227, v69
	v_readlane_b32 s59, v246, 2

; #define LAS __attribute__((address_space(3)))
; #define LDS_BARRIER() do { asm volatile("s_waitcnt lgkmcnt(0)" ::: "memory"); __builtin_amdgcn_s_barrier(); asm volatile("" ::: "memory"); } while (0)
; __device__ __forceinline__ void phase3_pool(const Args& a, LAS unsigned char* lds, int tid, int vcu, int G) {
;     ...
;     unsigned* ctr = (unsigned*)(a.ws + WS_CTL) + CTL_POOL_TICKET;
;     volatile LAS unsigned* tk = (volatile LAS unsigned*)(lds + LDS_MISC) + 16;
;     unsigned nxt = 0;
;     if (tid == 0) nxt = __hip_atomic_fetch_add(ctr, 1u, __ATOMIC_RELAXED, __HIP_MEMORY_SCOPE_AGENT);
;     for (;;) {
;         if (tid == 0) *tk = nxt;
;         LDS_BARRIER();
;         const int item = (int)*tk;
;         if (item >= 1024) break;
;         if (tid == 0) nxt = __hip_atomic_fetch_add(ctr, 1u, __ATOMIC_RELAXED, __HIP_MEMORY_SCOPE_AGENT);
.LBB0_673:
	s_cmp_lg_u32 s99, 0
	s_cbranch_scc1 .Lp3_after_pool
	s_add_u32 s42, s92, 0xea60
	s_addc_u32 s43, s93, 0
	v_mov_b32_e32 v1, 0
	v_cmp_eq_u32_e64 s[0:1], 0, v66
	s_and_saveexec_b64 s[2:3], s[0:1]
	s_cbranch_execz .LBB0_677
	s_mov_b64 s[6:7], exec
	v_mbcnt_lo_u32_b32 v1, s6, 0
	v_mbcnt_hi_u32_b32 v1, s7, v1
	v_cmp_eq_u32_e32 vcc, 0, v1
	s_and_saveexec_b64 s[4:5], vcc
	s_cbranch_execz .LBB0_676
	s_bcnt1_i32_b64 s6, s[6:7]
	v_mov_b32_e32 v2, 0
	v_mov_b32_e32 v3, s6

; #define LDS_BARRIER() do { asm volatile("s_waitcnt lgkmcnt(0)" ::: "memory"); __builtin_amdgcn_s_barrier(); asm volatile("" ::: "memory"); } while (0)
; __device__ __forceinline__ void phase3_pool(const Args& a, LAS unsigned char* lds, int tid, int vcu, int G) {
;     ...
;     for (;;) {
;         if (tid == 0) *tk = nxt;
;         LDS_BARRIER();
;         const int item = (int)*tk;
;         if (item >= 1024) break;
;         if (tid == 0) nxt = __hip_atomic_fetch_add(ctr, 1u, __ATOMIC_RELAXED, __HIP_MEMORY_SCOPE_AGENT);
;         const int g = item >> 8, r = (item >> 3) & 31, b = item & 7;
.LBB0_686:
	s_or_b64 exec, exec, s[4:5]
	s_add_i32 s4, s8, s97
	v_add_u32_e32 v1, s4, v1

; #define LDS_BARRIER() do { asm volatile("s_waitcnt lgkmcnt(0)" ::: "memory"); __builtin_amdgcn_s_barrier(); asm volatile("" ::: "memory"); } while (0)
; __device__ __forceinline__ unsigned xb_add(unsigned* p, unsigned v) { return __hip_atomic_fetch_add(p, v, __ATOMIC_RELAXED, __HIP_MEMORY_SCOPE_AGENT); }
; __device__ __forceinline__ void xcd_barrier(const XcdBarrier& b) {
;     asm volatile("s_waitcnt vmcnt(0)" ::: "memory");
;     __syncthreads();
;     if (threadIdx.x == 0) {
;         unsigned* bar = b.bar;
;         __builtin_amdgcn_s_waitcnt(0);
;         unsigned nloc = b.st[0], nx = b.st[1];
;         if (nloc == 0u) { xcd_barrier_complete(bar, b.x, nloc, nx); b.st[0] = nloc; b.st[1] = nx; }
;         const unsigned old = xb_add(&bar[XB_XSUB(b.x)], 1u);
; __device__ __forceinline__ void phase3_pool(const Args& a, LAS unsigned char* lds, int tid, int vcu, int G) {
;     ...
;     LDS_BARRIER();
.LBB0_714:
	s_waitcnt lgkmcnt(0)
	s_barrier
	s_cmp_lg_u32 s99, 0
	s_cbranch_scc1 .Lp3_after_pool
	s_mov_b32 s99, 1
	s_branch .Lp3_prep_start
.Lp3_after_pool:
	s_cmp_lt_i32 s95, 5
	s_cbranch_scc1 .LBB0_764
	s_waitcnt vmcnt(0)
	v_cmp_eq_u32_e32 vcc, 0, v0
	s_waitcnt vmcnt(0)
	s_barrier
	s_and_saveexec_b64 s[0:1], vcc
	s_cbranch_execz .LBB0_763
	v_readlane_b32 s2, v246, 22
	s_waitcnt vmcnt(0) expcnt(0) lgkmcnt(0)
	s_nop 0
	v_mov_b32_e32 v1, s2
	ds_read_b32 v3, v1
	ds_read_b32 v1, v1 offset:4
	s_waitcnt lgkmcnt(1)
	v_cmp_ne_u32_e32 vcc, 0, v3
	s_cbranch_vccnz .LBB0_731
	v_readlane_b32 s4, v246, 0
	v_readlane_b32 s5, v246, 1
	s_load_dwordx2 s[2:3], s[4:5], 0x4
	s_add_u32 s4, s92, 0x4200
	s_addc_u32 s5, s93, 0
	s_add_u32 s6, s92, 0x4400
	s_addc_u32 s7, s93, 0
	s_waitcnt lgkmcnt(0)
	s_mul_i32 s33, s2, s97
	s_add_u32 s2, s92, 0x4500
	s_mul_i32 s33, s33, s3
	s_addc_u32 s3, s93, 0
	s_add_u32 s8, s92, 0x4600
	s_addc_u32 s9, s93, 0
	s_add_u32 s10, s92, 0x4700
	s_addc_u32 s11, s93, 0
	s_add_u32 s12, s92, 0x4800
	s_addc_u32 s13, s93, 0
	s_add_u32 s14, s92, 0x4900
	s_addc_u32 s15, s93, 0
	s_add_u32 s16, s92, 0x4a00
	s_addc_u32 s17, s93, 0
	s_add_u32 s18, s92, 0x4b00
	s_addc_u32 s19, s93, 0
	s_add_u32 s20, s92, 0x4c00
	s_addc_u32 s21, s93, 0
	s_add_u32 s22, s92, 0x4d00
	s_addc_u32 s23, s93, 0
	s_add_u32 s24, s92, 0x4e00
	s_addc_u32 s25, s93, 0
	s_add_u32 s26, s92, 0x4f00
	s_addc_u32 s27, s93, 0
	s_add_u32 s28, s92, 0x5000
	s_addc_u32 s29, s93, 0
	s_add_u32 s30, s92, 0x5100
	s_addc_u32 s31, s93, 0
	s_add_u32 s34, s92, 0x5200
	s_addc_u32 s35, s93, 0
	s_add_u32 s42, s92, 0x5300
	s_addc_u32 s43, s93, 0
	s_mov_b32 s36, 1
	v_mov_b32_e32 v17, 0
	s_branch .LBB0_719

; #define RUNPH(k, ...) do { if (IN(k)) { { PH_IDS __VA_ARGS__ } if (REP_PHASE == (k)) { xcd_barrier(bar); { PH_IDS __VA_ARGS__ } } SEAM(k); } } while (0)
;     __device__ __forceinline__ bool next(int i, U& u) const {
;         const int nt = tile[3 * NTILE_MAX]; const int L = i * G + c; if (L >= nt * 4) return false;
;         const int t = L >> 2; u.pn = L & 3; const int e = tile[t]; u.row0 = tile[NTILE_MAX + t]; u.nrows = tile[2 * NTILE_MAX + t];
;         u.A = H2; u.B = W + ((size_t)e * 1024 + u.pn * 256) * 2048; return true;
; __global__ void __launch_bounds__(512, 2) fwd(Args args) {
;     ...
;     RUNPH(9, {
;         MoeGUSched S{(const char*)(ws + RA_H2), (const char*)(ws + WS_WGU), (const int*)(ws + T_TILE), (const int*)(ws + T_SLOTTOK), G, vcu};
;         EpiGU E{ws + WS_ACT, (const float*)(ws + T_SLOTW)};
;         int kgu = 1024; asm volatile("" : "+s"(kgu));
;         pg8::gemm_phase<EpiGU, MoeGUSched, true>(lds, kgu, S, E); });
.LBB0_1278:
	s_cmp_gt_i32 s94, 9
	s_cselect_b64 s[0:1], -1, 0
	s_cmp_lt_i32 s95, 10
	s_cselect_b64 s[2:3], -1, 0
	s_or_b64 s[0:1], s[0:1], s[2:3]
	s_and_b64 vcc, exec, s[0:1]
	s_waitcnt lgkmcnt(0)
	v_readlane_b32 s71, v246, 2
	v_readlane_b32 s72, v246, 22
	s_cbranch_vccnz .LBB0_1371
	v_mov_b32_e32 v1, v0
	s_movk_i32 s0, 0x400
	v_mov_b32_e32 v1, 0x39e72000
	global_load_dword v1, v1, s[92:93] offset:256
	s_add_u32 s10, s92, 0x1a200000
	s_addc_u32 s11, s93, 0
	s_add_u32 s33, s92, 0x9e00000
	s_addc_u32 s38, s93, 0
	s_add_u32 s39, s92, 0x39e70000
	s_addc_u32 s44, s93, 0
	s_add_u32 s12, s92, 0x39e72100
	s_addc_u32 s13, s93, 0
	v_readfirstlane_b32 s6, v0
	s_waitcnt vmcnt(0)
	v_readfirstlane_b32 s1, v1
	s_mov_b32 s98, s1
	s_lshl_b32 s1, s1, 2
	s_cmp_lt_i32 s71, s1
	s_cselect_b64 s[2:3], -1, 0
	s_cmp_ge_i32 s71, s1
	s_cbranch_scc1 .LBB0_1281
	s_ashr_i32 s4, s71, 2
	s_ashr_i32 s5, s4, 31
	s_and_b32 s65, s71, 3
	s_lshl_b64 s[4:5], s[4:5], 2
	s_add_u32 s4, s39, s4
	s_addc_u32 s5, s44, s5
	v_mov_b32_e32 v1, 0
	global_load_dword v2, v1, s[4:5]
	v_mov_b32_e32 v3, 0x1000
	global_load_dword v226, v1, s[4:5] offset:2816
	global_load_dword v227, v3, s[4:5] offset:1536
	s_lshl_b32 s1, s65, 19
	s_mov_b64 s[34:35], s[10:11]
	s_waitcnt vmcnt(2)
	v_readfirstlane_b32 s4, v2
	s_ashr_i32 s5, s4, 31
	s_lshl_b64 s[4:5], s[4:5], 21
	s_add_u32 s4, s33, s4
	s_addc_u32 s5, s38, s5
	s_add_u32 s4, s4, s1
	s_addc_u32 s5, s5, 0
	s_andn2_b64 vcc, exec, s[2:3]
	s_cbranch_vccz .LBB0_1282
	s_branch .LBB0_1321

; #define PG8_STAGE(bufoff, gbase, v0, v1) do { \
;         __builtin_amdgcn_global_load_lds((const unsigned*)((const char*)(gbase) + (v0)), (LAS unsigned*)(lds + (bufoff) + ldsw), 16, 0, 0); \
;         __builtin_amdgcn_global_load_lds((const unsigned*)((const char*)(gbase) + (v1)), (LAS unsigned*)(lds + (bufoff) + ldsw + 8192), 16, 0, 0); } while (0)
; #define PG8_WAIT_V(n) asm volatile("s_waitcnt vmcnt(" #n ")" ::: "memory")
; #define PG8_BAR __builtin_amdgcn_s_barrier()
; template <class Epi, class Sched, bool FP8 = false>
; __device__ __forceinline__ void gemm_phase(LAS unsigned char* lds, const int K, const Sched& S, const Epi& E) {
;     ...
;     PG8_STAGE(PG8_SB(0, 0), cB, voffB[0], voffB[1]); PG8_STAGE(PG8_SB(0, 1), cB + hstepB, voffB[0], voffB[1]); PG8_STAGE(PG8_SA(0, 0), cA, vA[0], vA[1]); PG8_STAGE(PG8_SA(0, 1), cA, vA[2], vA[3]);
;     if (wr == 1) PG8_BAR;
;     PG8_WAIT_V(2); PG8_BAR;
;     PG8_STAGE(PG8_SB(1, 0), cB + kstep, voffB[0], voffB[1]); PG8_STAGE(PG8_SA(1, 0), cA + kstep, vA[0], vA[1]); PG8_STAGE(PG8_SB(1, 1), cB + hstepB + kstep, voffB[0], voffB[1]);
;     PG8_WAIT_V(6); PG8_BAR;
;     __device__ __forceinline__ bool next(int i, U& u) const {
;         const int nt = tile[3 * NTILE_MAX]; const int L = i * G + c; if (L >= nt * 4) return false;
;         const int t = L >> 2; u.pn = L & 3; const int e = tile[t]; u.row0 = tile[NTILE_MAX + t]; u.nrows = tile[2 * NTILE_MAX + t];
.LBB0_1284:
	s_add_u32 s20, s92, 0x30b00000
	s_addc_u32 s21, s93, 0
	s_add_u32 s22, s92, 0x39dd0000
	s_mov_b64 s[24:25], 0x80
	s_addc_u32 s23, s93, 0
	v_lshl_add_u64 v[10:11], v[10:11], 0, s[24:25]
	s_add_i32 m0, s46, 0x18000
	s_waitcnt vmcnt(2)
	s_barrier
	global_load_lds_dwordx4 v[10:11], off
	v_lshl_add_u64 v[6:7], v[6:7], 0, s[24:25]
	s_add_i32 m0, s46, 0x1a000
	s_add_i32 s52, s46, 0x8000
	global_load_lds_dwordx4 v[6:7], off
	v_lshl_add_u64 v[6:7], v[8:9], 0, s[24:25]
	s_mov_b32 m0, s52
	s_add_i32 s53, s46, 0xa000
	global_load_lds_dwordx4 v[6:7], off
	v_lshl_add_u64 v[6:7], v[12:13], 0, s[24:25]
	s_mov_b32 m0, s53
	v_lshl_add_u64 v[4:5], v[4:5], 0, s[24:25]
	global_load_lds_dwordx4 v[6:7], off
	s_add_i32 m0, s46, 0x1c000
	v_lshl_add_u64 v[2:3], v[2:3], 0, s[24:25]
	global_load_lds_dwordx4 v[4:5], off
	s_add_i32 m0, s46, 0x1e000
	s_lshr_b32 s1, s1, 26
	global_load_lds_dwordx4 v[2:3], off
	v_lshlrev_b32_e32 v3, 6, v0
	s_add_i32 s1, s0, s1
	v_and_b32_e32 v2, 48, v0
	v_and_b32_e32 v3, 0x3c0, v3
	v_lshlrev_b32_e32 v5, 2, v0
	s_ashr_i32 s54, s1, 6
	v_or_b32_e32 v4, v3, v2
	s_lshl_b32 s1, s3, 13
	v_and_b32_e32 v5, 32, v5
	v_bitop3_b32 v2, v3, v5, v2 bitop3:0x36
	v_bitop3_b32 v3, s1, v4, v5 bitop3:0xf6
	s_lshl_b32 s1, s2, 12
	s_and_b32 s1, s1, 0x3000
	s_cmp_gt_i32 s0, 63
	v_or_b32_e32 v205, s1, v2
	s_cselect_b64 s[0:1], -1, 0
	s_add_i32 s55, s54, -2
	s_cmpk_lt_u32 s6, 0x100
	s_waitcnt vmcnt(6)
	s_cselect_b64 s[26:27], -1, 0
	s_add_i32 s60, 0, 0x10000
	s_add_i32 s62, 0, 0x14000
	v_cndmask_b32_e64 v2, 0, 1, s[0:1]
	v_add_u32_e32 v228, s60, v205
	v_add_u32_e32 v229, s62, v205
	s_mov_b32 s28, 0x39800000
	s_add_i32 s60, s60, s45
	s_add_i32 s62, s62, s45
	v_mov_b32_e32 v207, 0x1000
	v_cmp_ne_u32_e64 s[0:1], 1, v2
	v_add_u32_e32 v230, 0, v3
	s_movk_i32 s56, 0xffc0
	s_mov_b32 s29, 0x41800000
	s_mov_b32 s57, 0xc3e00000
	s_add_i32 s58, s46, 0xc000
	s_add_i32 s59, s46, 0xe000
	s_add_i32 s61, s60, 0x2000
	s_add_i32 s63, s62, 0x2000
	v_mov_b32_e32 v231, 0x43e00000
	s_mov_b64 s[30:31], s[4:5]
	s_mov_b64 s[36:37], s[34:35]
	s_barrier
	s_add_i32 s73, s97, s71
	s_ashr_i32 s73, s73, 2
	s_lshl_b32 s73, s73, 2
	s_add_u32 s74, s39, s73
	s_addc_u32 s75, s44, 0
	s_load_dword s76, s[74:75], 0x0
	s_load_dword s77, s[74:75], 0xb00
	s_load_dword s78, s[74:75], 0x1600
	s_branch .LBB0_1287

;     __device__ __forceinline__ void aoffs(const U& u, const int (&R)[2], const int (&C)[2], unsigned (&v)[4]) const { D.aoffs(u, R, C, v); }
; template <class Epi, class Sched, bool FP8 = false>
; __device__ __forceinline__ void gemm_phase(LAS unsigned char* lds, const int K, const Sched& S, const Epi& E) {
;     ...
;         const bool has_next = S.next(ui + 1, nxt);
;         const bool lo_only = S.lo_only(cur);
;         const char* nA = has_next ? nxt.A : cA; const char* nB = has_next ? nxt.B : cB;
;         if (has_next) S.aoffs(nxt, R, C, vN); else { vN[0] = vA[0]; vN[1] = vA[1]; vN[2] = vA[2]; vN[3] = vA[3]; }
;     __device__ __forceinline__ bool next(int i, U& u) const {
;         const int nt = tile[3 * NTILE_MAX]; const int L = i * G + c; if (L >= nt * 4) return false;
;         const int t = L >> 2; u.pn = L & 3; const int e = tile[t]; u.row0 = tile[NTILE_MAX + t]; u.nrows = tile[2 * NTILE_MAX + t];
;         u.A = H2; u.B = W + ((size_t)e * 1024 + u.pn * 256) * 2048; return true;
;     }
;     __device__ __forceinline__ void aoffs(const U& u, const int (&R)[2], const int (&C)[2], unsigned (&v)[4]) const {
; #pragma unroll
;         for (int h = 0; h < 2; ++h)
; #pragma unroll
;             for (int i = 0; i < 2; ++i) { int r = h * 128 + R[i]; r = r < u.nrows ? r : u.nrows - 1; const int tok = slot_tok[u.row0 + r]; v[h * 2 + i] = (unsigned)(tok * 1024 + C[i]) * 2u; }
.LBB0_1287:
	s_add_i32 s51, s51, 1
	s_mul_i32 s2, s51, s97
	s_add_i32 s2, s2, s71
	s_lshl_b32 s3, s98, 2
	s_cmp_lt_i32 s2, s3
	s_cselect_b64 s[6:7], -1, 0
	s_waitcnt lgkmcnt(0)
	s_cmp_ge_i32 s2, s3
	s_cbranch_scc1 .Lp9_nonext
	s_and_b32 s64, s2, 3
	v_mov_b32_e32 v233, s77
	v_mov_b32_e32 v232, s78
	s_lshl_b32 s8, s64, 19
	s_mov_b64 s[36:37], s[10:11]
	s_mov_b32 s2, s76
	s_ashr_i32 s3, s2, 31
	s_lshl_b64 s[2:3], s[2:3], 21
	s_add_u32 s2, s33, s2
	s_addc_u32 s3, s38, s3
	s_add_u32 s30, s2, s8
	s_addc_u32 s31, s3, 0
	s_branch .Lp9_gather
.Lp9_nonext:
	v_mov_b32_e32 v233, v226
	v_mov_b32_e32 v232, v227
.Lp9_gather:
	v_cndmask_b32_e64 v2, 0, 1, s[6:7]
	v_cmp_ne_u32_e64 s[2:3], 1, v2
	v_add_u32_e32 v8, -1, v232
	v_min_i32_e32 v2, v1, v8
	v_min_i32_e32 v4, v222, v8
	v_add_u32_e32 v2, v2, v233
	v_add_u32_e32 v4, v4, v233
	v_min_i32_e32 v6, v223, v8
	v_min_i32_e32 v8, v224, v8
	v_ashrrev_i32_e32 v3, 31, v2
	v_ashrrev_i32_e32 v5, 31, v4
	v_add_u32_e32 v6, v6, v233
	v_add_u32_e32 v8, v8, v233
	v_lshl_add_u64 v[2:3], v[2:3], 2, s[14:15]
	v_lshl_add_u64 v[4:5], v[4:5], 2, s[14:15]
	v_ashrrev_i32_e32 v7, 31, v6
	v_ashrrev_i32_e32 v9, 31, v8
	v_lshl_add_u64 v[6:7], v[6:7], 2, s[14:15]
	v_lshl_add_u64 v[8:9], v[8:9], 2, s[14:15]
	global_load_dword v240, v[2:3], off
	global_load_dword v241, v[4:5], off
	global_load_dword v242, v[6:7], off
	global_load_dword v243, v[8:9], off

; #define PG8_WAIT_V(n) asm volatile("s_waitcnt vmcnt(" #n ")" ::: "memory")
; #define PG8_WAIT_L(n) asm volatile("s_waitcnt lgkmcnt(" #n ")" ::: "memory")
; template <class Epi, class Sched, bool FP8 = false>
; __device__ __forceinline__ void gemm_phase(LAS unsigned char* lds, const int K, const Sched& S, const Epi& E) {
;     ...
;         if (has_next) S.aoffs(nxt, R, C, vN); else { vN[0] = vA[0]; vN[1] = vA[1]; vN[2] = vA[2]; vN[3] = vA[3]; }
;         for (int t = 0; t < nt; t += 2) {
;             const bool last = (t == nt - 2);
;             const char* a1 = cA + (size_t)(t + 1) * kstep;
;             const char* a2 = last ? nA : cA + (size_t)(t + 2) * kstep; const char* b2 = last ? nB : cB + (size_t)(t + 2) * kstep;
;             const char* a3 = a2 + kstep; const char* b3 = b2 + kstep;
;             const unsigned x0 = last ? vN[0] : vA[0], x1 = last ? vN[1] : vA[1], x2 = last ? vN[2] : vA[2], x3 = last ? vN[3] : vA[3];
;             PG8_LDB(B0, 0, 0); PG8_LDB(B1, 0, 1); PG8_SCHED; PG8_LDA(At, 0, 0); PG8_STAGE(PG8_SA(1, 1), a1, vA[2], vA[3]);
;             PG8_WAIT_V(8); PG8_WAIT_L(0); PG8_BAR; PG8_MMA(0, 0, At, B0); PG8_MMA(0, 1, At, B1); PG8_BAR; PG8_SCHED;
;             PG8_LDA(At, 0, 1); PG8_STAGE(PG8_SB(0, 0), b2, voffB[0], voffB[1]); PG8_STAGE(PG8_SB(0, 1), b2 + hstepB, voffB[0], voffB[1]); PG8_STAGE(PG8_SA(0, 0), a2, x0, x1);
;             PG8_WAIT_V(8); PG8_WAIT_L(0); PG8_BAR; if (!lo_only) { PG8_MMA(1, 0, At, B0); PG8_MMA(1, 1, At, B1); } PG8_BAR; PG8_SCHED;
;             PG8_LDB(B0, 1, 0); PG8_LDB(B1, 1, 1); PG8_SCHED; PG8_LDA(At, 1, 0); PG8_STAGE(PG8_SA(0, 1), a2, x2, x3);
;             PG8_WAIT_V(8); PG8_WAIT_L(0); PG8_BAR; PG8_MMA(0, 0, At, B0); PG8_MMA(0, 1, At, B1); PG8_BAR; PG8_SCHED;
;             PG8_LDA(At, 1, 1); PG8_STAGE(PG8_SB(1, 0), b3, voffB[0], voffB[1]); PG8_STAGE(PG8_SB(1, 1), b3 + hstepB, voffB[0], voffB[1]); PG8_STAGE(PG8_SA(1, 0), a3, x0, x1);
;             PG8_WAIT_V(8); PG8_WAIT_L(0); PG8_BAR; if (!lo_only) { PG8_MMA(1, 0, At, B0); PG8_MMA(1, 1, At, B1); } PG8_BAR; PG8_SCHED;
;     __device__ __forceinline__ void aoffs(const U& u, const int (&R)[2], const int (&C)[2], unsigned (&v)[4]) const {
;     ...
;             for (int i = 0; i < 2; ++i) { int r = h * 128 + R[i]; r = r < u.nrows ? r : u.nrows - 1; const int tok = slot_tok[u.row0 + r]; v[h * 2 + i] = (unsigned)(tok * 1024 + C[i]) * 2u; }
.LBB0_1296:
	v_lshl_or_b32 v234, v240, 11, v225
	v_lshl_or_b32 v235, v241, 11, v225
	v_lshl_or_b32 v236, v242, 11, v225
	v_lshl_or_b32 v237, v243, 11, v225
	v_mov_b32_e32 v69, v67
	v_lshl_add_u64 v[238:239], s[42:43], 0, v[66:67]
	v_lshl_add_u64 v[68:69], s[42:43], 0, v[68:69]
	v_cndmask_b32_e64 v66, v202, v236, s[6:7]
	v_cndmask_b32_e64 v209, v208, v237, s[6:7]
	s_barrier
	s_add_i32 s6, 0, 0x18000
	s_add_i32 s7, 0, 0x1c000
	v_add_u32_e32 v2, s6, v205
	v_add_u32_e32 v14, s7, v205
	ds_read_b128 v[18:21], v2
	ds_read_b128 v[22:25], v2 offset:1024
	ds_read_b128 v[26:29], v2 offset:2048
	ds_read_b128 v[30:33], v2 offset:3072
	ds_read_b128 v[2:5], v14
	ds_read_b128 v[6:9], v14 offset:1024
	ds_read_b128 v[10:13], v14 offset:2048
	ds_read_b128 v[14:17], v14 offset:3072
	s_mov_b32 m0, s48
	s_waitcnt lgkmcnt(0)
	ds_read_b128 v[34:37], v230 offset:32768
	ds_read_b128 v[38:41], v230 offset:33792
	ds_read_b128 v[42:45], v230 offset:34816
	ds_read_b128 v[46:49], v230 offset:35840
	ds_read_b128 v[50:53], v230 offset:36864
	ds_read_b128 v[54:57], v230 offset:37888
	ds_read_b128 v[58:61], v230 offset:38912
	ds_read_b128 v[62:65], v230 offset:39936
	global_load_lds_dwordx4 v66, s[42:43]
	s_mov_b32 m0, s49
	s_nop 0
	global_load_lds_dwordx4 v209, s[42:43]
	s_waitcnt vmcnt(8)
	s_waitcnt lgkmcnt(0)
	s_barrier
	s_setprio 1
	s_nop 4
	s_waitcnt lgkmcnt(0)
	v_mfma_f32_16x16x128_f8f6f4 v[186:189], v[18:25], v[34:41], v[186:189]
	v_mfma_f32_16x16x128_f8f6f4 v[182:185], v[26:33], v[34:41], v[182:185]
	v_mfma_f32_16x16x128_f8f6f4 v[170:173], v[18:25], v[42:49], v[170:173]
	v_mfma_f32_16x16x128_f8f6f4 v[166:169], v[26:33], v[42:49], v[166:169]
	v_mfma_f32_16x16x128_f8f6f4 v[154:157], v[18:25], v[50:57], v[154:157]
	v_mfma_f32_16x16x128_f8f6f4 v[150:153], v[26:33], v[50:57], v[150:153]
	v_mfma_f32_16x16x128_f8f6f4 v[138:141], v[18:25], v[58:65], v[138:141]
	v_mfma_f32_16x16x128_f8f6f4 v[134:137], v[26:33], v[58:65], v[134:137]
	s_setprio 0
	s_setprio 1
	s_nop 4
	v_mfma_f32_16x16x128_f8f6f4 v[194:197], v[2:9], v[34:41], v[194:197]
	v_mfma_f32_16x16x128_f8f6f4 v[190:193], v[10:17], v[34:41], v[190:193]
	v_mfma_f32_16x16x128_f8f6f4 v[178:181], v[2:9], v[42:49], v[178:181]
	v_mfma_f32_16x16x128_f8f6f4 v[174:177], v[10:17], v[42:49], v[174:177]
	v_mfma_f32_16x16x128_f8f6f4 v[162:165], v[2:9], v[50:57], v[162:165]
	v_mfma_f32_16x16x128_f8f6f4 v[158:161], v[10:17], v[50:57], v[158:161]
	v_mfma_f32_16x16x128_f8f6f4 v[146:149], v[2:9], v[58:65], v[146:149]
	v_mfma_f32_16x16x128_f8f6f4 v[142:145], v[10:17], v[58:65], v[142:145]
	s_setprio 0
	s_barrier
	s_add_i32 s6, s6, s45
	v_lshl_add_u64 v[216:217], v[216:217], 0, s[24:25]
	s_mov_b32 m0, s6
	ds_read_b128 v[58:61], v230 offset:49152
	ds_read_b128 v[62:65], v230 offset:50176
	ds_read_b128 v[50:53], v230 offset:51200
	ds_read_b128 v[54:57], v230 offset:52224
	ds_read_b128 v[42:45], v230 offset:53248
	ds_read_b128 v[46:49], v230 offset:54272
	ds_read_b128 v[34:37], v230 offset:55296
	ds_read_b128 v[38:41], v230 offset:56320
	global_load_lds_dwordx4 v[216:217], off
	v_lshl_add_u64 v[214:215], v[214:215], 0, s[24:25]
	s_add_i32 m0, s6, 0x2000
	s_add_i32 s6, s7, s45
	global_load_lds_dwordx4 v[214:215], off
	v_lshl_add_u64 v[214:215], v[220:221], 0, s[24:25]
	s_mov_b32 m0, s6
	v_lshl_add_u64 v[68:69], v[68:69], 0, s[24:25]
	global_load_lds_dwordx4 v[214:215], off
	v_lshl_add_u64 v[214:215], v[218:219], 0, s[24:25]
	s_add_i32 m0, s6, 0x2000
	s_and_b64 vcc, exec, s[8:9]
	global_load_lds_dwordx4 v[214:215], off
	v_lshl_add_u64 v[214:215], v[238:239], 0, s[24:25]
	s_mov_b32 m0, s52
	s_nop 0
	global_load_lds_dwordx4 v[214:215], off
	s_mov_b32 m0, s53
	s_nop 0
	global_load_lds_dwordx4 v[68:69], off
	s_waitcnt vmcnt(8)
	s_waitcnt lgkmcnt(0)
	s_barrier
	s_cbranch_vccnz .LBB0_1293
	s_setprio 1
	s_nop 4
	s_waitcnt lgkmcnt(0)
	v_mfma_f32_16x16x128_f8f6f4 v[122:125], v[18:25], v[58:65], v[122:125]
	v_mfma_f32_16x16x128_f8f6f4 v[118:121], v[26:33], v[58:65], v[118:121]
	v_mfma_f32_16x16x128_f8f6f4 v[106:109], v[18:25], v[50:57], v[106:109]
	v_mfma_f32_16x16x128_f8f6f4 v[102:105], v[26:33], v[50:57], v[102:105]
	v_mfma_f32_16x16x128_f8f6f4 v[90:93], v[18:25], v[42:49], v[90:93]
	v_mfma_f32_16x16x128_f8f6f4 v[86:89], v[26:33], v[42:49], v[86:89]
	v_mfma_f32_16x16x128_f8f6f4 v[74:77], v[18:25], v[34:41], v[74:77]
	v_mfma_f32_16x16x128_f8f6f4 v[70:73], v[26:33], v[34:41], v[70:73]
	s_setprio 0
	s_setprio 1
	s_nop 4
	v_mfma_f32_16x16x128_f8f6f4 v[130:133], v[2:9], v[58:65], v[130:133]
	v_mfma_f32_16x16x128_f8f6f4 v[126:129], v[10:17], v[58:65], v[126:129]
	v_mfma_f32_16x16x128_f8f6f4 v[114:117], v[2:9], v[50:57], v[114:117]
	v_mfma_f32_16x16x128_f8f6f4 v[110:113], v[10:17], v[50:57], v[110:113]
	v_mfma_f32_16x16x128_f8f6f4 v[98:101], v[2:9], v[42:49], v[98:101]
	v_mfma_f32_16x16x128_f8f6f4 v[94:97], v[10:17], v[42:49], v[94:97]
	v_mfma_f32_16x16x128_f8f6f4 v[82:85], v[2:9], v[34:41], v[82:85]
	v_mfma_f32_16x16x128_f8f6f4 v[78:81], v[10:17], v[34:41], v[78:81]
	s_setprio 0
	s_branch .LBB0_1293

; __device__ __forceinline__ float silu_f(float x) { return x * __builtin_amdgcn_rcpf(1.f + __expf(-x)); }
;     __device__ __forceinline__ bool next(int i, U& u) const {
;         const int nt = tile[3 * NTILE_MAX]; const int L = i * G + c; if (L >= nt * 4) return false;
;         const int t = L >> 2; u.pn = L & 3; const int e = tile[t]; u.row0 = tile[NTILE_MAX + t]; u.nrows = tile[2 * NTILE_MAX + t];
;     __device__ __forceinline__ void operator()(const f32x4 (&acc)[2][2][4][2], const MoeU& u, int wr, int wc, int fr, int fq) const {
;         const int c0 = u.pn * 128 + wc * 32 + 8 * fq; constexpr float inv = 1.f / (SC_W * SC_H);
; #pragma unroll
;         for (int ai = 0; ai < 2; ++ai)
; #pragma unroll
;             for (int m = 0; m < 4; ++m) { const int r = ai * 128 + wr * 64 + m * 16 + fr;
;                 if (r < u.nrows) { const float w = slot_w[u.row0 + r] * SC_A; float o[8];
; #pragma unroll
;                     for (int n = 0; n < 2; ++n)
; #pragma unroll
;                         for (int j = 0; j < 4; ++j) { const float g = acc[ai][0][m][n][j] * inv, up = acc[ai][1][m][n][j] * inv; o[n * 4 + j] = silu_f(g) * up * w; }
;                     v2u q; q.x = pk4_fp8(o[0], o[1], o[2], o[3]); q.y = pk4_fp8(o[4], o[5], o[6], o[7]);
;                     *(v2u*)(act + (size_t)(u.row0 + r) * 512 + c0) = q; } }
.LBB0_1301:
	s_add_i32 s73, s51, 1
	s_mul_i32 s73, s73, s97
	s_add_i32 s73, s73, s71
	s_ashr_i32 s73, s73, 2
	s_lshl_b32 s73, s73, 2
	s_add_u32 s74, s39, s73
	s_addc_u32 s75, s44, 0
	s_load_dword s76, s[74:75], 0x0
	s_load_dword s77, s[74:75], 0xb00
	s_load_dword s78, s[74:75], 0x1600
	v_mov_b32_e32 v3, v0
	s_nop 15
	s_nop 15
	s_nop 0
	v_lshrrev_b32_e32 v2, 1, v3
	v_and_b32_e32 v4, 15, v3
	v_and_b32_e32 v2, 0x78, v2
	v_ashrrev_i32_e32 v3, 2, v3
	v_lshl_or_b32 v2, s65, 7, v2
	v_and_or_b32 v4, v3, s56, v4
	v_ashrrev_i32_e32 v3, 31, v2
	v_cmp_lt_i32_e32 vcc, v4, v227
	s_and_saveexec_b64 s[4:5], vcc
	s_cbranch_execz .LBB0_1303
	v_add_u32_e32 v6, v4, v226
	v_ashrrev_i32_e32 v7, 31, v6
	v_lshl_add_u64 v[8:9], v[6:7], 2, s[22:23]
	global_load_dword v9, v[8:9], off
	v_mov_b32_e32 v10, v194
	v_mov_b32_e32 v11, v186
	v_mov_b32_e32 v186, v195
	v_mov_b32_e32 v12, v196
	v_mov_b32_e32 v13, v188
	v_mov_b32_e32 v188, v197
	v_mov_b32_e32 v14, v190
	v_mov_b32_e32 v15, v182
	v_mov_b32_e32 v182, v191
	v_mul_f32_e32 v5, 0x39800000, v184
	v_mov_b32_e32 v184, v193
	v_pk_mul_f32 v[10:11], v[10:11], s[28:29] op_sel_hi:[1,0]
	v_pk_mul_f32 v[18:19], v[186:187], s[28:29] op_sel_hi:[1,0]
	v_pk_mul_f32 v[12:13], v[12:13], s[28:29] op_sel_hi:[1,0]
	v_pk_mul_f32 v[20:21], v[188:189], s[28:29] op_sel_hi:[1,0]
	v_pk_mul_f32 v[14:15], v[14:15], s[28:29] op_sel_hi:[1,0]
	v_pk_mul_f32 v[22:23], v[182:183], s[28:29] op_sel_hi:[1,0]
	v_pk_mul_f32 v[24:25], v[184:185], s[28:29] op_sel_hi:[1,0]
	v_mul_f32_e32 v27, 0xbfb8aa3b, v11
	v_mul_f32_e32 v28, 0xbfb8aa3b, v19
	v_mul_f32_e32 v26, 0xbfb8aa3b, v5
	v_mul_f32_e32 v29, 0xbfb8aa3b, v13
	v_mul_f32_e32 v30, 0xbfb8aa3b, v21
	v_mul_f32_e32 v31, 0xbfb8aa3b, v15
	v_mul_f32_e32 v32, 0xbfb8aa3b, v23
	v_mul_f32_e32 v33, 0xbfb8aa3b, v25
	v_exp_f32_e32 v27, v27
	v_exp_f32_e32 v28, v28
	v_exp_f32_e32 v26, v26
	v_exp_f32_e32 v29, v29
	v_exp_f32_e32 v30, v30
	v_exp_f32_e32 v31, v31
	v_exp_f32_e32 v32, v32
	v_exp_f32_e32 v33, v33
	v_add_f32_e32 v27, 1.0, v27
	v_add_f32_e32 v28, 1.0, v28
	v_add_f32_e32 v26, 1.0, v26
	v_add_f32_e32 v29, 1.0, v29
	v_add_f32_e32 v30, 1.0, v30
	v_add_f32_e32 v31, 1.0, v31
	v_add_f32_e32 v32, 1.0, v32
	v_add_f32_e32 v33, 1.0, v33
	v_rcp_f32_e32 v27, v27
	v_rcp_f32_e32 v28, v28
	v_rcp_f32_e32 v26, v26
	v_rcp_f32_e32 v29, v29
	v_rcp_f32_e32 v30, v30
	v_rcp_f32_e32 v31, v31
	v_rcp_f32_e32 v32, v32
	v_rcp_f32_e32 v33, v33
	v_mov_b32_e32 v8, v192
	v_mul_f32_e32 v11, v11, v27
	v_mul_f32_e32 v19, v19, v28
	v_mul_f32_e32 v5, v5, v26
	v_mul_f32_e32 v13, v13, v29
	v_mul_f32_e32 v21, v21, v30
	v_mul_f32_e32 v15, v15, v31
	v_mul_f32_e32 v23, v23, v32
	v_mul_f32_e32 v25, v25, v33
	v_mul_f32_e32 v10, v10, v11
	v_mul_f32_e32 v11, v18, v19
	v_mul_f32_e32 v12, v12, v13
	v_mul_f32_e32 v13, v20, v21
	v_mul_f32_e32 v14, v14, v15
	v_mul_f32_e32 v15, v22, v23
	v_mul_f32_e32 v18, v24, v25
	v_mov_b32_e32 v16, v67
	v_mov_b32_e32 v17, v67
	v_lshlrev_b64 v[6:7], 9, v[6:7]
	v_lshl_add_u64 v[6:7], s[20:21], 0, v[6:7]
	v_lshl_add_u64 v[6:7], v[6:7], 0, v[2:3]
	s_waitcnt vmcnt(0)
	v_pk_mul_f32 v[8:9], v[8:9], s[28:29]
	s_nop 0
	v_mul_f32_e32 v10, v10, v9
	v_mul_f32_e32 v11, v11, v9
	v_mul_f32_e32 v5, v8, v5
	v_mul_f32_e32 v12, v12, v9
	v_mul_f32_e32 v13, v13, v9
	v_mul_f32_e32 v14, v14, v9
	v_mul_f32_e32 v15, v15, v9
	v_mul_f32_e32 v8, v18, v9
	v_mul_f32_e32 v5, v5, v9
	v_med3_f32 v9, v10, s57, v231
	v_med3_f32 v10, v11, s57, v231
	v_cvt_pk_fp8_f32 v16, v9, v10
	v_med3_f32 v9, v14, s57, v231
	v_med3_f32 v10, v15, s57, v231
	v_cvt_pk_fp8_f32 v17, v9, v10
	v_med3_f32 v11, v12, s57, v231
	v_med3_f32 v12, v13, s57, v231
	v_med3_f32 v5, v5, s57, v231
	v_med3_f32 v8, v8, s57, v231
	v_cvt_pk_fp8_f32 v16, v11, v12 op_sel:[0,0,1]
	v_cvt_pk_fp8_f32 v17, v5, v8 op_sel:[0,0,1]
	global_store_dwordx2 v[6:7], v[16:17], off
